# baseline (speedup 1.0000x reference)
.Lu0_2:
	s_waitcnt lgkmcnt(14)
	v_mfma_f32_32x32x16_f16 v[2:17], v[158:161], v[178:181], v[2:17]
	v_exp_f32_e32 v98, v98
	v_exp_f32_e32 v99, v99
	v_exp_f32_e32 v100, v100
	v_exp_f32_e32 v101, v101
	s_waitcnt lgkmcnt(12)
	v_mfma_f32_32x32x16_f16 v[18:33], v[158:161], v[174:177], v[18:33]
	v_exp_f32_e32 v102, v102
	v_exp_f32_e32 v103, v103
	v_exp_f32_e32 v104, v104
	v_exp_f32_e32 v105, v105
	ds_read_b128 v[58:61], v211 offset:16384
	ds_read_b128 v[114:117], v211 offset:20480
	s_waitcnt lgkmcnt(12)
	v_mfma_f32_32x32x16_f16 v[2:17], v[150:153], v[170:173], v[2:17]
	v_exp_f32_e32 v106, v106
	v_exp_f32_e32 v107, v107
	v_exp_f32_e32 v108, v108
	v_exp_f32_e32 v109, v109
	ds_read_b128 v[182:185], v210 offset:16384
	ds_read_b128 v[174:177], v210 offset:20480
	s_waitcnt lgkmcnt(12)
	v_mfma_f32_32x32x16_f16 v[18:33], v[150:153], v[74:77], v[18:33]
	v_exp_f32_e32 v110, v110
	v_exp_f32_e32 v111, v111
	v_exp_f32_e32 v112, v112
	v_exp_f32_e32 v113, v113
	ds_read_b128 v[178:181], v209 offset:16384
	ds_read_b128 v[166:169], v209 offset:20480
	s_waitcnt lgkmcnt(12)
	v_mfma_f32_32x32x16_f16 v[2:17], v[142:145], v[70:73], v[2:17]
	v_exp_f32_e32 v82, v82
	v_exp_f32_e32 v83, v83
	v_exp_f32_e32 v84, v84
	v_exp_f32_e32 v85, v85
	ds_read_b128 v[170:173], v208 offset:16384
	ds_read_b128 v[162:165], v208 offset:20480
	s_waitcnt lgkmcnt(12)
	v_mfma_f32_32x32x16_f16 v[18:33], v[142:145], v[66:69], v[18:33]
	v_exp_f32_e32 v86, v86
	v_exp_f32_e32 v87, v87
	v_exp_f32_e32 v88, v88
	v_exp_f32_e32 v89, v89
	s_waitcnt lgkmcnt(10)
	v_mfma_f32_32x32x16_f16 v[2:17], v[130:133], v[54:57], v[2:17]
	v_exp_f32_e32 v90, v90
	v_exp_f32_e32 v91, v91
	v_exp_f32_e32 v92, v92
	v_exp_f32_e32 v93, v93
	s_waitcnt lgkmcnt(8)
	v_mfma_f32_32x32x16_f16 v[18:33], v[130:133], v[50:53], v[18:33]
	v_exp_f32_e32 v94, v94
	v_exp_f32_e32 v95, v95
	v_exp_f32_e32 v96, v96
	v_exp_f32_e32 v97, v97
	s_waitcnt vmcnt(2) lgkmcnt(0)
	s_barrier
	s_cmp_eq_u64 s[26:27], 0
	s_cbranch_scc0 .Lu0_resc1

.Lu0_5:
	s_waitcnt lgkmcnt(14)
	v_mfma_f32_32x32x16_f16 v[2:17], v[158:161], v[126:129], v[2:17]
	v_exp_f32_e32 v66, v66
	v_exp_f32_e32 v67, v67
	v_exp_f32_e32 v68, v68
	v_exp_f32_e32 v69, v69
	s_waitcnt lgkmcnt(12)
	v_mfma_f32_32x32x16_f16 v[18:33], v[158:161], v[122:125], v[18:33]
	v_exp_f32_e32 v70, v70
	v_exp_f32_e32 v71, v71
	v_exp_f32_e32 v72, v72
	v_exp_f32_e32 v73, v73
	ds_read_b128 v[82:85], v211
	ds_read_b128 v[170:173], v211 offset:4096
	s_waitcnt lgkmcnt(12)
	v_mfma_f32_32x32x16_f16 v[2:17], v[150:153], v[118:121], v[2:17]
	v_exp_f32_e32 v74, v74
	v_exp_f32_e32 v75, v75
	v_exp_f32_e32 v76, v76
	v_exp_f32_e32 v77, v77
	ds_read_b128 v[166:169], v210
	ds_read_b128 v[162:165], v210 offset:4096
	s_waitcnt lgkmcnt(12)
	v_mfma_f32_32x32x16_f16 v[18:33], v[150:153], v[114:117], v[18:33]
	v_exp_f32_e32 v78, v78
	v_exp_f32_e32 v79, v79
	v_exp_f32_e32 v80, v80
	v_exp_f32_e32 v81, v81
	ds_read_b128 v[126:129], v209
	ds_read_b128 v[122:125], v209 offset:4096
	s_waitcnt lgkmcnt(12)
	v_mfma_f32_32x32x16_f16 v[2:17], v[142:145], v[106:109], v[2:17]
	v_exp_f32_e32 v50, v50
	v_exp_f32_e32 v51, v51
	v_exp_f32_e32 v52, v52
	v_exp_f32_e32 v53, v53
	ds_read_b128 v[118:121], v208
	ds_read_b128 v[114:117], v208 offset:4096
	s_waitcnt lgkmcnt(12)
	v_mfma_f32_32x32x16_f16 v[18:33], v[142:145], v[102:105], v[18:33]
	v_exp_f32_e32 v54, v54
	v_exp_f32_e32 v55, v55
	v_exp_f32_e32 v56, v56
	v_exp_f32_e32 v57, v57
	s_waitcnt lgkmcnt(10)
	v_mfma_f32_32x32x16_f16 v[2:17], v[130:133], v[98:101], v[2:17]
	v_exp_f32_e32 v58, v58
	v_exp_f32_e32 v59, v59
	v_exp_f32_e32 v60, v60
	v_exp_f32_e32 v61, v61
	s_waitcnt lgkmcnt(8)
	v_mfma_f32_32x32x16_f16 v[18:33], v[130:133], v[86:89], v[18:33]
	v_exp_f32_e32 v62, v62
	v_exp_f32_e32 v63, v63
	v_exp_f32_e32 v64, v64
	v_exp_f32_e32 v65, v65
	s_waitcnt vmcnt(2) lgkmcnt(0)
	s_barrier
	s_cmp_eq_u64 s[26:27], 0
	s_cbranch_scc0 .Lu0_resc2
.Lu0_7:
	s_add_u32 s50, s50, 0x4000
	s_addc_u32 s51, s51, 0
	s_add_u32 s52, s52, 0x4000
	s_addc_u32 s53, s53, 0
	s_add_i32 s26, s43, 0x2000
	s_cmpk_lg_i32 s43, 0x4000
	s_cselect_b32 s27, s26, 0
	s_add_i32 s40, s40, 2
	s_cmp_lt_u32 s40, 25
	s_cbranch_scc0 .LBB2_15
	s_mov_b32 s26, s39
	s_mov_b32 s42, s43
	s_mov_b32 s39, s27
.Lu1_1:
	ds_read_b64_tr_b16 v[178:179], v206 offset:40960
	ds_read_b64_tr_b16 v[180:181], v206 offset:41984
	s_waitcnt lgkmcnt(9)
	v_mfma_f32_32x32x16_f16 v[98:113], v[82:85], v[154:157], v[34:49]
	v_add_f32_e32 v86, v66, v67
	v_add_f32_e32 v86, v68, v86
	v_add_f32_e32 v86, v69, v86
	v_add_f32_e32 v86, v70, v86
	v_add_f32_e32 v86, v71, v86
	v_cvt_pk_f16_f32 v158, v66, v67
	v_cvt_pk_f16_f32 v159, v68, v69
	ds_read_b64_tr_b16 v[174:175], v207 offset:40960
	ds_read_b64_tr_b16 v[176:177], v207 offset:41984
	v_add_f32_e32 v66, v72, v86
	s_waitcnt lgkmcnt(10)
	v_mfma_f32_32x32x16_f16 v[82:97], v[170:173], v[154:157], v[34:49]
	v_add_f32_e32 v66, v73, v66
	v_add_f32_e32 v66, v74, v66
	v_add_f32_e32 v66, v75, v66
	v_cvt_pk_f16_f32 v160, v70, v71
	v_cvt_pk_f16_f32 v161, v72, v73
	ds_read_b64_tr_b16 v[170:171], v206 offset:43008
	ds_read_b64_tr_b16 v[172:173], v206 offset:44032
	s_waitcnt lgkmcnt(11)
	v_mfma_f32_32x32x16_f16 v[98:113], v[166:169], v[146:149], v[98:113]
	v_add_f32_e32 v66, v76, v66
	v_add_f32_e32 v66, v77, v66
	v_add_f32_e32 v66, v78, v66
	v_add_f32_e32 v66, v79, v66
	v_cvt_pk_f16_f32 v150, v74, v75
	v_cvt_pk_f16_f32 v151, v76, v77
	ds_read_b64_tr_b16 v[74:75], v207 offset:43008
	ds_read_b64_tr_b16 v[76:77], v207 offset:44032
	s_waitcnt lgkmcnt(12)
	v_mfma_f32_32x32x16_f16 v[82:97], v[162:165], v[146:149], v[82:97]
	v_add_f32_e32 v66, v80, v66
	v_add_f32_e32 v66, v81, v66
	v_add_f32_e32 v66, v50, v66
	v_add_f32_e32 v66, v51, v66
	v_cvt_pk_f16_f32 v152, v78, v79
	v_cvt_pk_f16_f32 v153, v80, v81
	ds_read_b64_tr_b16 v[70:71], v206 offset:45056
	ds_read_b64_tr_b16 v[72:73], v206 offset:46080
	s_waitcnt lgkmcnt(13)
	v_mfma_f32_32x32x16_f16 v[98:113], v[126:129], v[138:141], v[98:113]
	v_add_f32_e32 v66, v52, v66
	v_add_f32_e32 v66, v53, v66
	v_add_f32_e32 v66, v54, v66
	v_add_f32_e32 v78, v55, v66
	v_cvt_pk_f16_f32 v142, v50, v51
	v_cvt_pk_f16_f32 v143, v52, v53
	ds_read_b64_tr_b16 v[66:67], v207 offset:45056
	ds_read_b64_tr_b16 v[68:69], v207 offset:46080
	s_waitcnt lgkmcnt(14)
	v_mfma_f32_32x32x16_f16 v[82:97], v[122:125], v[138:141], v[82:97]
	v_add_f32_e32 v50, v56, v78
	v_add_f32_e32 v50, v57, v50
	v_add_f32_e32 v50, v58, v50
	v_add_f32_e32 v50, v59, v50
	v_cvt_pk_f16_f32 v144, v54, v55
	v_cvt_pk_f16_f32 v145, v56, v57
	ds_read_b64_tr_b16 v[54:55], v206 offset:47104
	ds_read_b64_tr_b16 v[56:57], v206 offset:48128
	s_waitcnt lgkmcnt(14)
	v_mfma_f32_32x32x16_f16 v[98:113], v[118:121], v[134:137], v[98:113]
	v_add_f32_e32 v50, v60, v50
	v_add_f32_e32 v50, v61, v50
	v_add_f32_e32 v50, v62, v50
	v_add_f32_e32 v78, v63, v50
	v_cvt_pk_f16_f32 v130, v58, v59
	v_cvt_pk_f16_f32 v131, v60, v61
	ds_read_b64_tr_b16 v[50:51], v207 offset:47104
	ds_read_b64_tr_b16 v[52:53], v207 offset:48128
	v_mfma_f32_32x32x16_f16 v[82:97], v[114:117], v[134:137], v[82:97]
	v_add_f32_e32 v58, v64, v78
	v_add_f32_e32 v60, v65, v58
	v_cvt_pk_f16_f32 v132, v62, v63
	v_cvt_pk_f16_f32 v133, v64, v65
	s_add_i32 s26, s42, s36
	s_mov_b32 m0, s26
	s_nop 0
	global_load_lds_dwordx4 v221, s[50:51]
	s_add_i32 s26, s39, s35
	s_mov_b32 m0, s26
	s_nop 0
	global_load_lds_dwordx4 v222, s[52:53]
	v_max_f32_e32 v58, v98, v99
	v_max3_f32 v59, v100, v101, v83
	v_max3_f32 v58, v58, v82, v84
	v_max3_f32 v58, v58, v85, v102
	v_max3_f32 v59, v59, v104, v105
	v_max3_f32 v58, v58, v103, v86
	v_max3_f32 v59, v59, v88, v89
	v_max3_f32 v58, v58, v87, v106
	v_max3_f32 v59, v59, v108, v109
	v_max3_f32 v58, v58, v107, v90
	v_max3_f32 v59, v59, v92, v93
	v_max3_f32 v58, v58, v91, v110
	v_max3_f32 v59, v59, v112, v113
	v_max3_f32 v58, v58, v111, v94
	v_max3_f32 v59, v59, v96, v97
	v_max3_f32 v58, v58, v95, v59
	v_mov_b32_e32 v59, v58
	v_add_f32_e32 v198, v183, v60
	s_nop 0
	v_permlane32_swap_b32_e32 v58, v59
	v_max_f32_e32 v58, v58, v59
	v_cmp_lt_f32_e32 vcc, s41, v58
	s_cmp_lg_u64 vcc, 0
	s_cselect_b64 s[26:27], -1, 0
	s_cbranch_vccnz .Lu1_9
.Lu1_2:
	s_waitcnt lgkmcnt(14)
	v_mfma_f32_32x32x16_f16 v[2:17], v[158:161], v[178:181], v[2:17]
	v_exp_f32_e32 v98, v98
	v_exp_f32_e32 v99, v99
	v_exp_f32_e32 v100, v100
	v_exp_f32_e32 v101, v101
	s_waitcnt lgkmcnt(12)
	v_mfma_f32_32x32x16_f16 v[18:33], v[158:161], v[174:177], v[18:33]
	v_exp_f32_e32 v102, v102
	v_exp_f32_e32 v103, v103
	v_exp_f32_e32 v104, v104
	v_exp_f32_e32 v105, v105
	ds_read_b128 v[58:61], v211 offset:8192
	ds_read_b128 v[114:117], v211 offset:12288
	s_waitcnt lgkmcnt(12)
	v_mfma_f32_32x32x16_f16 v[2:17], v[150:153], v[170:173], v[2:17]
	v_exp_f32_e32 v106, v106
	v_exp_f32_e32 v107, v107
	v_exp_f32_e32 v108, v108
	v_exp_f32_e32 v109, v109
	ds_read_b128 v[182:185], v210 offset:8192
	ds_read_b128 v[174:177], v210 offset:12288
	s_waitcnt lgkmcnt(12)
	v_mfma_f32_32x32x16_f16 v[18:33], v[150:153], v[74:77], v[18:33]
	v_exp_f32_e32 v110, v110
	v_exp_f32_e32 v111, v111
	v_exp_f32_e32 v112, v112
	v_exp_f32_e32 v113, v113
	ds_read_b128 v[178:181], v209 offset:8192
	ds_read_b128 v[166:169], v209 offset:12288
	s_waitcnt lgkmcnt(12)
	v_mfma_f32_32x32x16_f16 v[2:17], v[142:145], v[70:73], v[2:17]
	v_exp_f32_e32 v82, v82
	v_exp_f32_e32 v83, v83
	v_exp_f32_e32 v84, v84
	v_exp_f32_e32 v85, v85
	ds_read_b128 v[170:173], v208 offset:8192
	ds_read_b128 v[162:165], v208 offset:12288
	s_waitcnt lgkmcnt(12)
	v_mfma_f32_32x32x16_f16 v[18:33], v[142:145], v[66:69], v[18:33]
	v_exp_f32_e32 v86, v86
	v_exp_f32_e32 v87, v87
	v_exp_f32_e32 v88, v88
	v_exp_f32_e32 v89, v89
	s_waitcnt lgkmcnt(10)
	v_mfma_f32_32x32x16_f16 v[2:17], v[130:133], v[54:57], v[2:17]
	v_exp_f32_e32 v90, v90
	v_exp_f32_e32 v91, v91
	v_exp_f32_e32 v92, v92
	v_exp_f32_e32 v93, v93
	s_waitcnt lgkmcnt(8)
	v_mfma_f32_32x32x16_f16 v[18:33], v[130:133], v[50:53], v[18:33]
	v_exp_f32_e32 v94, v94
	v_exp_f32_e32 v95, v95
	v_exp_f32_e32 v96, v96
	v_exp_f32_e32 v97, v97
	s_waitcnt vmcnt(2) lgkmcnt(0)
	s_barrier
	s_cmp_eq_u64 s[26:27], 0
	s_cbranch_scc0 .Lu1_resc1

.Lu1_5:
	s_waitcnt lgkmcnt(14)
	v_mfma_f32_32x32x16_f16 v[2:17], v[158:161], v[126:129], v[2:17]
	v_exp_f32_e32 v66, v66
	v_exp_f32_e32 v67, v67
	v_exp_f32_e32 v68, v68
	v_exp_f32_e32 v69, v69
	s_waitcnt lgkmcnt(12)
	v_mfma_f32_32x32x16_f16 v[18:33], v[158:161], v[122:125], v[18:33]
	v_exp_f32_e32 v70, v70
	v_exp_f32_e32 v71, v71
	v_exp_f32_e32 v72, v72
	v_exp_f32_e32 v73, v73
	ds_read_b128 v[82:85], v211 offset:16384
	ds_read_b128 v[170:173], v211 offset:20480
	s_waitcnt lgkmcnt(12)
	v_mfma_f32_32x32x16_f16 v[2:17], v[150:153], v[118:121], v[2:17]
	v_exp_f32_e32 v74, v74
	v_exp_f32_e32 v75, v75
	v_exp_f32_e32 v76, v76
	v_exp_f32_e32 v77, v77
	ds_read_b128 v[166:169], v210 offset:16384
	ds_read_b128 v[162:165], v210 offset:20480
	s_waitcnt lgkmcnt(12)
	v_mfma_f32_32x32x16_f16 v[18:33], v[150:153], v[114:117], v[18:33]
	v_exp_f32_e32 v78, v78
	v_exp_f32_e32 v79, v79
	v_exp_f32_e32 v80, v80
	v_exp_f32_e32 v81, v81
	ds_read_b128 v[126:129], v209 offset:16384
	ds_read_b128 v[122:125], v209 offset:20480
	s_waitcnt lgkmcnt(12)
	v_mfma_f32_32x32x16_f16 v[2:17], v[142:145], v[106:109], v[2:17]
	v_exp_f32_e32 v50, v50
	v_exp_f32_e32 v51, v51
	v_exp_f32_e32 v52, v52
	v_exp_f32_e32 v53, v53
	ds_read_b128 v[118:121], v208 offset:16384
	ds_read_b128 v[114:117], v208 offset:20480
	s_waitcnt lgkmcnt(12)
	v_mfma_f32_32x32x16_f16 v[18:33], v[142:145], v[102:105], v[18:33]
	v_exp_f32_e32 v54, v54
	v_exp_f32_e32 v55, v55
	v_exp_f32_e32 v56, v56
	v_exp_f32_e32 v57, v57
	s_waitcnt lgkmcnt(10)
	v_mfma_f32_32x32x16_f16 v[2:17], v[130:133], v[98:101], v[2:17]
	v_exp_f32_e32 v58, v58
	v_exp_f32_e32 v59, v59
	v_exp_f32_e32 v60, v60
	v_exp_f32_e32 v61, v61
	s_waitcnt lgkmcnt(8)
	v_mfma_f32_32x32x16_f16 v[18:33], v[130:133], v[86:89], v[18:33]
	v_exp_f32_e32 v62, v62
	v_exp_f32_e32 v63, v63
	v_exp_f32_e32 v64, v64
	v_exp_f32_e32 v65, v65
	s_waitcnt vmcnt(2) lgkmcnt(0)
	s_barrier
	s_cmp_eq_u64 s[26:27], 0
	s_cbranch_scc0 .Lu1_resc2
.Lu1_7:
	s_add_u32 s50, s50, 0x4000
	s_addc_u32 s51, s51, 0
	s_add_u32 s52, s52, 0x4000
	s_addc_u32 s53, s53, 0
	s_add_i32 s26, s43, 0x2000
	s_cmpk_lg_i32 s43, 0x4000
	s_cselect_b32 s27, s26, 0
	s_add_i32 s40, s40, 2
	s_cmp_lt_u32 s40, 25
	s_cbranch_scc0 .LBB2_15
	s_mov_b32 s26, s39
	s_mov_b32 s42, s43
	s_mov_b32 s39, s27
.Lu2_1:
	ds_read_b64_tr_b16 v[178:179], v206 offset:32768
	ds_read_b64_tr_b16 v[180:181], v206 offset:33792
	s_waitcnt lgkmcnt(9)
	v_mfma_f32_32x32x16_f16 v[98:113], v[82:85], v[154:157], v[34:49]
	v_add_f32_e32 v86, v66, v67
	v_add_f32_e32 v86, v68, v86
	v_add_f32_e32 v86, v69, v86
	v_add_f32_e32 v86, v70, v86
	v_add_f32_e32 v86, v71, v86
	v_cvt_pk_f16_f32 v158, v66, v67
	v_cvt_pk_f16_f32 v159, v68, v69
	ds_read_b64_tr_b16 v[174:175], v207 offset:32768
	ds_read_b64_tr_b16 v[176:177], v207 offset:33792
	v_add_f32_e32 v66, v72, v86
	s_waitcnt lgkmcnt(10)
	v_mfma_f32_32x32x16_f16 v[82:97], v[170:173], v[154:157], v[34:49]
	v_add_f32_e32 v66, v73, v66
	v_add_f32_e32 v66, v74, v66
	v_add_f32_e32 v66, v75, v66
	v_cvt_pk_f16_f32 v160, v70, v71
	v_cvt_pk_f16_f32 v161, v72, v73
	ds_read_b64_tr_b16 v[170:171], v206 offset:34816
	ds_read_b64_tr_b16 v[172:173], v206 offset:35840
	s_waitcnt lgkmcnt(11)
	v_mfma_f32_32x32x16_f16 v[98:113], v[166:169], v[146:149], v[98:113]
	v_add_f32_e32 v66, v76, v66
	v_add_f32_e32 v66, v77, v66
	v_add_f32_e32 v66, v78, v66
	v_add_f32_e32 v66, v79, v66
	v_cvt_pk_f16_f32 v150, v74, v75
	v_cvt_pk_f16_f32 v151, v76, v77
	ds_read_b64_tr_b16 v[74:75], v207 offset:34816
	ds_read_b64_tr_b16 v[76:77], v207 offset:35840
	s_waitcnt lgkmcnt(12)
	v_mfma_f32_32x32x16_f16 v[82:97], v[162:165], v[146:149], v[82:97]
	v_add_f32_e32 v66, v80, v66
	v_add_f32_e32 v66, v81, v66
	v_add_f32_e32 v66, v50, v66
	v_add_f32_e32 v66, v51, v66
	v_cvt_pk_f16_f32 v152, v78, v79
	v_cvt_pk_f16_f32 v153, v80, v81
	ds_read_b64_tr_b16 v[70:71], v206 offset:36864
	ds_read_b64_tr_b16 v[72:73], v206 offset:37888
	s_waitcnt lgkmcnt(13)
	v_mfma_f32_32x32x16_f16 v[98:113], v[126:129], v[138:141], v[98:113]
	v_add_f32_e32 v66, v52, v66
	v_add_f32_e32 v66, v53, v66
	v_add_f32_e32 v66, v54, v66
	v_add_f32_e32 v78, v55, v66
	v_cvt_pk_f16_f32 v142, v50, v51
	v_cvt_pk_f16_f32 v143, v52, v53
	ds_read_b64_tr_b16 v[66:67], v207 offset:36864
	ds_read_b64_tr_b16 v[68:69], v207 offset:37888
	s_waitcnt lgkmcnt(14)
	v_mfma_f32_32x32x16_f16 v[82:97], v[122:125], v[138:141], v[82:97]
	v_add_f32_e32 v50, v56, v78
	v_add_f32_e32 v50, v57, v50
	v_add_f32_e32 v50, v58, v50
	v_add_f32_e32 v50, v59, v50
	v_cvt_pk_f16_f32 v144, v54, v55
	v_cvt_pk_f16_f32 v145, v56, v57
	ds_read_b64_tr_b16 v[54:55], v206 offset:38912
	ds_read_b64_tr_b16 v[56:57], v206 offset:39936
	s_waitcnt lgkmcnt(14)
	v_mfma_f32_32x32x16_f16 v[98:113], v[118:121], v[134:137], v[98:113]
	v_add_f32_e32 v50, v60, v50
	v_add_f32_e32 v50, v61, v50
	v_add_f32_e32 v50, v62, v50
	v_add_f32_e32 v78, v63, v50
	v_cvt_pk_f16_f32 v130, v58, v59
	v_cvt_pk_f16_f32 v131, v60, v61
	ds_read_b64_tr_b16 v[50:51], v207 offset:38912
	ds_read_b64_tr_b16 v[52:53], v207 offset:39936
	v_mfma_f32_32x32x16_f16 v[82:97], v[114:117], v[134:137], v[82:97]
	v_add_f32_e32 v58, v64, v78
	v_add_f32_e32 v60, v65, v58
	v_cvt_pk_f16_f32 v132, v62, v63
	v_cvt_pk_f16_f32 v133, v64, v65
	s_add_i32 s26, s42, s36
	s_mov_b32 m0, s26
	s_nop 0
	global_load_lds_dwordx4 v221, s[50:51]
	s_add_i32 s26, s39, s35
	s_mov_b32 m0, s26
	s_nop 0
	global_load_lds_dwordx4 v222, s[52:53]
	v_max_f32_e32 v58, v98, v99
	v_max3_f32 v59, v100, v101, v83
	v_max3_f32 v58, v58, v82, v84
	v_max3_f32 v58, v58, v85, v102
	v_max3_f32 v59, v59, v104, v105
	v_max3_f32 v58, v58, v103, v86
	v_max3_f32 v59, v59, v88, v89
	v_max3_f32 v58, v58, v87, v106
	v_max3_f32 v59, v59, v108, v109
	v_max3_f32 v58, v58, v107, v90
	v_max3_f32 v59, v59, v92, v93
	v_max3_f32 v58, v58, v91, v110
	v_max3_f32 v59, v59, v112, v113
	v_max3_f32 v58, v58, v111, v94
	v_max3_f32 v59, v59, v96, v97
	v_max3_f32 v58, v58, v95, v59
	v_mov_b32_e32 v59, v58
	v_add_f32_e32 v198, v183, v60
	s_nop 0
	v_permlane32_swap_b32_e32 v58, v59
	v_max_f32_e32 v58, v58, v59
	v_cmp_lt_f32_e32 vcc, s41, v58
	s_cmp_lg_u64 vcc, 0
	s_cselect_b64 s[26:27], -1, 0
	s_cbranch_vccnz .Lu2_9
.Lu2_2:
	s_waitcnt lgkmcnt(14)
	v_mfma_f32_32x32x16_f16 v[2:17], v[158:161], v[178:181], v[2:17]
	v_exp_f32_e32 v98, v98
	v_exp_f32_e32 v99, v99
	v_exp_f32_e32 v100, v100
	v_exp_f32_e32 v101, v101
	s_waitcnt lgkmcnt(12)
	v_mfma_f32_32x32x16_f16 v[18:33], v[158:161], v[174:177], v[18:33]
	v_exp_f32_e32 v102, v102
	v_exp_f32_e32 v103, v103
	v_exp_f32_e32 v104, v104
	v_exp_f32_e32 v105, v105
	ds_read_b128 v[58:61], v211
	ds_read_b128 v[114:117], v211 offset:4096
	s_waitcnt lgkmcnt(12)
	v_mfma_f32_32x32x16_f16 v[2:17], v[150:153], v[170:173], v[2:17]
	v_exp_f32_e32 v106, v106
	v_exp_f32_e32 v107, v107
	v_exp_f32_e32 v108, v108
	v_exp_f32_e32 v109, v109
	ds_read_b128 v[182:185], v210
	ds_read_b128 v[174:177], v210 offset:4096
	s_waitcnt lgkmcnt(12)
	v_mfma_f32_32x32x16_f16 v[18:33], v[150:153], v[74:77], v[18:33]
	v_exp_f32_e32 v110, v110
	v_exp_f32_e32 v111, v111
	v_exp_f32_e32 v112, v112
	v_exp_f32_e32 v113, v113
	ds_read_b128 v[178:181], v209
	ds_read_b128 v[166:169], v209 offset:4096
	s_waitcnt lgkmcnt(12)
	v_mfma_f32_32x32x16_f16 v[2:17], v[142:145], v[70:73], v[2:17]
	v_exp_f32_e32 v82, v82
	v_exp_f32_e32 v83, v83
	v_exp_f32_e32 v84, v84
	v_exp_f32_e32 v85, v85
	ds_read_b128 v[170:173], v208
	ds_read_b128 v[162:165], v208 offset:4096
	s_waitcnt lgkmcnt(12)
	v_mfma_f32_32x32x16_f16 v[18:33], v[142:145], v[66:69], v[18:33]
	v_exp_f32_e32 v86, v86
	v_exp_f32_e32 v87, v87
	v_exp_f32_e32 v88, v88
	v_exp_f32_e32 v89, v89
	s_waitcnt lgkmcnt(10)
	v_mfma_f32_32x32x16_f16 v[2:17], v[130:133], v[54:57], v[2:17]
	v_exp_f32_e32 v90, v90
	v_exp_f32_e32 v91, v91
	v_exp_f32_e32 v92, v92
	v_exp_f32_e32 v93, v93
	s_waitcnt lgkmcnt(8)
	v_mfma_f32_32x32x16_f16 v[18:33], v[130:133], v[50:53], v[18:33]
	v_exp_f32_e32 v94, v94
	v_exp_f32_e32 v95, v95
	v_exp_f32_e32 v96, v96
	v_exp_f32_e32 v97, v97
	s_waitcnt vmcnt(2) lgkmcnt(0)
	s_barrier
	s_cmp_eq_u64 s[26:27], 0
	s_cbranch_scc0 .Lu2_resc1

.Lu2_5:
	s_waitcnt lgkmcnt(14)
	v_mfma_f32_32x32x16_f16 v[2:17], v[158:161], v[126:129], v[2:17]
	v_exp_f32_e32 v66, v66
	v_exp_f32_e32 v67, v67
	v_exp_f32_e32 v68, v68
	v_exp_f32_e32 v69, v69
	s_waitcnt lgkmcnt(12)
	v_mfma_f32_32x32x16_f16 v[18:33], v[158:161], v[122:125], v[18:33]
	v_exp_f32_e32 v70, v70
	v_exp_f32_e32 v71, v71
	v_exp_f32_e32 v72, v72
	v_exp_f32_e32 v73, v73
	ds_read_b128 v[82:85], v211 offset:8192
	ds_read_b128 v[170:173], v211 offset:12288
	s_waitcnt lgkmcnt(12)
	v_mfma_f32_32x32x16_f16 v[2:17], v[150:153], v[118:121], v[2:17]
	v_exp_f32_e32 v74, v74
	v_exp_f32_e32 v75, v75
	v_exp_f32_e32 v76, v76
	v_exp_f32_e32 v77, v77
	ds_read_b128 v[166:169], v210 offset:8192
	ds_read_b128 v[162:165], v210 offset:12288
	s_waitcnt lgkmcnt(12)
	v_mfma_f32_32x32x16_f16 v[18:33], v[150:153], v[114:117], v[18:33]
	v_exp_f32_e32 v78, v78
	v_exp_f32_e32 v79, v79
	v_exp_f32_e32 v80, v80
	v_exp_f32_e32 v81, v81
	ds_read_b128 v[126:129], v209 offset:8192
	ds_read_b128 v[122:125], v209 offset:12288
	s_waitcnt lgkmcnt(12)
	v_mfma_f32_32x32x16_f16 v[2:17], v[142:145], v[106:109], v[2:17]
	v_exp_f32_e32 v50, v50
	v_exp_f32_e32 v51, v51
	v_exp_f32_e32 v52, v52
	v_exp_f32_e32 v53, v53
	ds_read_b128 v[118:121], v208 offset:8192
	ds_read_b128 v[114:117], v208 offset:12288
	s_waitcnt lgkmcnt(12)
	v_mfma_f32_32x32x16_f16 v[18:33], v[142:145], v[102:105], v[18:33]
	v_exp_f32_e32 v54, v54
	v_exp_f32_e32 v55, v55
	v_exp_f32_e32 v56, v56
	v_exp_f32_e32 v57, v57
	s_waitcnt lgkmcnt(10)
	v_mfma_f32_32x32x16_f16 v[2:17], v[130:133], v[98:101], v[2:17]
	v_exp_f32_e32 v58, v58
	v_exp_f32_e32 v59, v59
	v_exp_f32_e32 v60, v60
	v_exp_f32_e32 v61, v61
	s_waitcnt lgkmcnt(8)
	v_mfma_f32_32x32x16_f16 v[18:33], v[130:133], v[86:89], v[18:33]
	v_exp_f32_e32 v62, v62
	v_exp_f32_e32 v63, v63
	v_exp_f32_e32 v64, v64
	v_exp_f32_e32 v65, v65
	s_waitcnt vmcnt(2) lgkmcnt(0)
	s_barrier
	s_cmp_eq_u64 s[26:27], 0
	s_cbranch_scc0 .Lu2_resc2

.Lu0_resc1:
	s_waitcnt lgkmcnt(0)
	v_add_u32_e32 v66, s38, v212
	ds_read_b128 v[50:53], v66 offset:49248
	ds_read_b128 v[54:57], v66 offset:49216
	ds_read_b128 v[62:65], v66 offset:49184
	ds_read_b128 v[66:69], v66 offset:49152
	s_waitcnt lgkmcnt(3)
	v_pk_mul_f32 v[14:15], v[14:15], v[50:51]
	s_waitcnt lgkmcnt(2)
	v_pk_mul_f32 v[10:11], v[10:11], v[54:55]
	s_waitcnt lgkmcnt(1)
	v_pk_mul_f32 v[6:7], v[6:7], v[62:63]
	v_pk_mul_f32 v[16:17], v[16:17], v[52:53]
	v_pk_mul_f32 v[12:13], v[12:13], v[56:57]
	v_pk_mul_f32 v[8:9], v[8:9], v[64:65]
	s_waitcnt lgkmcnt(0)
	v_pk_mul_f32 v[4:5], v[4:5], v[68:69]
	v_pk_mul_f32 v[2:3], v[2:3], v[66:67]
	v_pk_mul_f32 v[30:31], v[30:31], v[50:51]
	v_pk_mul_f32 v[26:27], v[26:27], v[54:55]
	v_pk_mul_f32 v[22:23], v[22:23], v[62:63]
	v_pk_mul_f32 v[32:33], v[32:33], v[52:53]
	v_pk_mul_f32 v[28:29], v[28:29], v[56:57]
	v_pk_mul_f32 v[24:25], v[24:25], v[64:65]
	v_pk_mul_f32 v[20:21], v[20:21], v[68:69]
	v_pk_mul_f32 v[18:19], v[18:19], v[66:67]
	s_branch .Lu0_4
.Lu0_resc2:
	s_waitcnt lgkmcnt(0)
	v_add_u32_e32 v98, s38, v212
	ds_read_b128 v[86:89], v98 offset:49248
	ds_read_b128 v[90:93], v98 offset:49216
	ds_read_b128 v[94:97], v98 offset:49152
	ds_read_b128 v[98:101], v98 offset:49184
	s_waitcnt lgkmcnt(3)
	v_pk_mul_f32 v[16:17], v[16:17], v[88:89]
	v_pk_mul_f32 v[14:15], v[14:15], v[86:87]
	s_waitcnt lgkmcnt(2)
	v_pk_mul_f32 v[12:13], v[12:13], v[92:93]
	v_pk_mul_f32 v[10:11], v[10:11], v[90:91]
	s_waitcnt lgkmcnt(0)
	v_pk_mul_f32 v[8:9], v[8:9], v[100:101]
	v_pk_mul_f32 v[6:7], v[6:7], v[98:99]
	v_pk_mul_f32 v[4:5], v[4:5], v[96:97]
	v_pk_mul_f32 v[2:3], v[2:3], v[94:95]
	v_pk_mul_f32 v[32:33], v[32:33], v[88:89]
	v_pk_mul_f32 v[30:31], v[30:31], v[86:87]
	v_pk_mul_f32 v[28:29], v[28:29], v[92:93]
	v_pk_mul_f32 v[26:27], v[26:27], v[90:91]
	v_pk_mul_f32 v[24:25], v[24:25], v[100:101]
	v_pk_mul_f32 v[22:23], v[22:23], v[98:99]
	v_pk_mul_f32 v[20:21], v[20:21], v[96:97]
	v_pk_mul_f32 v[18:19], v[18:19], v[94:95]
	s_branch .Lu0_7
